# phase I: first K-loop iteration of each unit peeled, its first K-tile MFMAs take C=0, the 128 accumulator clears per unit are gone from the VALU-bound epilogue
# baseline (speedup 1.0000x reference)
.LBB0_856:
	s_ashr_i32 s65, s64, 31
	s_lshl_b64 s[8:9], s[64:65], 18
	s_add_u32 s66, s72, s8
	s_addc_u32 s67, s73, s9
	s_and_b64 s[8:9], s[38:39], exec
	s_cselect_b32 s4, s67, s1
	s_cselect_b32 s7, s66, s0
	s_lshl_b32 s8, s22, 10
	s_add_i32 s8, s8, 0
	s_add_i32 s8, s8, 0x20000
	v_lshl_add_u32 v196, v186, 2, s8
	v_lshl_add_u32 v197, v188, 2, s8
	s_add_u32 s8, s0, 0x100
	v_mov_b32_e32 v169, v49
	v_mov_b32_e32 v173, v49
	s_addc_u32 s9, s1, 0
	s_mov_b32 s10, -2
	s_mov_b64 s[70:71], s[60:61]
	s_cmp_eq_u32 s10, 4
	s_cselect_b64 s[0:1], -1, 0
	s_and_b64 s[12:13], s[38:39], s[0:1]
	s_andn2_b64 vcc, exec, s[12:13]
	v_mov_b64_e32 v[174:175], v[172:173]
	v_mov_b64_e32 v[176:177], v[168:169]
	v_mov_b32_e32 v182, v170
	v_mov_b32_e32 v48, v166
	s_add_u32 s12, s70, 0x80
	s_addc_u32 s13, s71, 0
	s_and_b64 s[0:1], s[0:1], exec
	s_cselect_b32 s37, s55, s13
	s_cselect_b32 s36, s54, s12
	s_cselect_b32 s1, s4, s9
	s_cselect_b32 s0, s7, s8
	s_add_i32 s13, 0, 0x10000
	s_add_i32 s12, 0, 0x14000
	v_add_u32_e32 v0, s13, v192
	v_add_u32_e32 v4, s12, v192
	ds_read_b128 v[24:27], v0
	ds_read_b128 v[28:31], v0 offset:1024
	ds_read_b128 v[16:19], v0 offset:2048
	ds_read_b128 v[20:23], v0 offset:3072
	ds_read_b128 v[8:11], v4
	ds_read_b128 v[12:15], v4 offset:1024
	ds_read_b128 v[0:3], v4 offset:2048
	ds_read_b128 v[4:7], v4 offset:3072
	v_lshl_add_u64 v[178:179], s[70:71], 0, v[168:169]
	s_add_i32 m0, s74, 0xc000
	ds_read_b128 v[206:209], v193
	ds_read_b128 v[210:213], v193 offset:1024
	ds_read_b128 v[214:217], v193 offset:2048
	ds_read_b128 v[218:221], v193 offset:3072
	ds_read_b128 v[240:243], v193 offset:4096
	ds_read_b128 v[244:247], v193 offset:5120
	ds_read_b128 v[198:201], v193 offset:6144
	ds_read_b128 v[202:205], v193 offset:7168
	global_load_lds_dwordx4 v[178:179], off
	v_lshl_add_u64 v[178:179], s[70:71], 0, v[172:173]
	s_add_i32 m0, s74, 0xe000
	s_nop 0
	global_load_lds_dwordx4 v[178:179], off
	s_waitcnt vmcnt(8)
	s_waitcnt lgkmcnt(0)
	s_barrier
	s_setprio 1
	s_waitcnt lgkmcnt(0)
	v_mfma_f32_16x16x128_f8f6f4 v[158:161], v[24:31], v[206:213], 0
	v_mfma_f32_16x16x128_f8f6f4 v[150:153], v[16:23], v[206:213], 0
	v_mfma_f32_16x16x128_f8f6f4 v[142:145], v[24:31], v[214:221], 0
	v_mfma_f32_16x16x128_f8f6f4 v[134:137], v[16:23], v[214:221], 0
	v_mfma_f32_16x16x128_f8f6f4 v[126:129], v[24:31], v[240:247], 0
	v_mfma_f32_16x16x128_f8f6f4 v[118:121], v[16:23], v[240:247], 0
	v_mfma_f32_16x16x128_f8f6f4 v[110:113], v[24:31], v[198:205], 0
	v_mfma_f32_16x16x128_f8f6f4 v[102:105], v[16:23], v[198:205], 0
	s_setprio 0
	s_setprio 1
	v_mfma_f32_16x16x128_f8f6f4 v[154:157], v[8:15], v[206:213], 0
	v_mfma_f32_16x16x128_f8f6f4 v[146:149], v[0:7], v[206:213], 0
	v_mfma_f32_16x16x128_f8f6f4 v[138:141], v[8:15], v[214:221], 0
	v_mfma_f32_16x16x128_f8f6f4 v[130:133], v[0:7], v[214:221], 0
	v_mfma_f32_16x16x128_f8f6f4 v[122:125], v[8:15], v[240:247], 0
	v_mfma_f32_16x16x128_f8f6f4 v[114:117], v[0:7], v[240:247], 0
	v_mfma_f32_16x16x128_f8f6f4 v[106:109], v[8:15], v[198:205], 0
	v_mfma_f32_16x16x128_f8f6f4 v[98:101], v[0:7], v[198:205], 0
	s_setprio 0
	s_barrier
	s_add_i32 s13, s13, s49
	v_lshl_add_u64 v[178:179], s[0:1], 0, v[162:163]
	s_mov_b32 m0, s13
	ds_read_b128 v[198:201], v193 offset:16384
	ds_read_b128 v[202:205], v193 offset:17408
	ds_read_b128 v[206:209], v193 offset:18432
	ds_read_b128 v[210:213], v193 offset:19456
	ds_read_b128 v[214:217], v193 offset:20480
	ds_read_b128 v[218:221], v193 offset:21504
	ds_read_b128 v[240:243], v193 offset:22528
	ds_read_b128 v[244:247], v193 offset:23552
	global_load_lds_dwordx4 v[178:179], off
	s_add_i32 m0, s13, 0x2000
	s_add_u32 s18, s0, 0x20000
	v_lshl_add_u64 v[180:181], s[0:1], 0, v[164:165]
	s_addc_u32 s19, s1, 0
	s_add_i32 s12, s12, s49
	global_load_lds_dwordx4 v[180:181], off
	v_lshl_add_u64 v[184:185], s[18:19], 0, v[162:163]
	s_mov_b32 m0, s12
	v_mov_b32_e32 v183, v49
	global_load_lds_dwordx4 v[184:185], off
	v_lshl_add_u64 v[184:185], s[18:19], 0, v[164:165]
	s_add_i32 m0, s12, 0x2000
	s_nop 0
	global_load_lds_dwordx4 v[184:185], off
	s_mov_b32 m0, s74
	v_lshl_add_u64 v[184:185], s[36:37], 0, v[48:49]
	global_load_lds_dwordx4 v48, s[36:37]
	s_mov_b32 m0, s75
	s_nop 0
	global_load_lds_dwordx4 v182, s[36:37]
	s_waitcnt vmcnt(8)
	s_waitcnt lgkmcnt(0)
	v_lshl_add_u64 v[182:183], s[36:37], 0, v[182:183]
	s_barrier
	s_setprio 1
	s_waitcnt lgkmcnt(0)
	v_mfma_f32_16x16x128_f8f6f4 v[94:97], v[24:31], v[198:205], 0
	v_mfma_f32_16x16x128_f8f6f4 v[86:89], v[16:23], v[198:205], 0
	v_mfma_f32_16x16x128_f8f6f4 v[78:81], v[24:31], v[206:213], 0
	v_mfma_f32_16x16x128_f8f6f4 v[70:73], v[16:23], v[206:213], 0
	v_mfma_f32_16x16x128_f8f6f4 v[62:65], v[24:31], v[214:221], 0
	v_mfma_f32_16x16x128_f8f6f4 v[54:57], v[16:23], v[214:221], 0
	v_mfma_f32_16x16x128_f8f6f4 v[44:47], v[24:31], v[240:247], 0
	v_mfma_f32_16x16x128_f8f6f4 v[36:39], v[16:23], v[240:247], 0
	s_setprio 0
	s_setprio 1
	v_mfma_f32_16x16x128_f8f6f4 v[90:93], v[8:15], v[198:205], 0
	v_mfma_f32_16x16x128_f8f6f4 v[82:85], v[0:7], v[198:205], 0
	v_mfma_f32_16x16x128_f8f6f4 v[74:77], v[8:15], v[206:213], 0
	v_mfma_f32_16x16x128_f8f6f4 v[66:69], v[0:7], v[206:213], 0
	v_mfma_f32_16x16x128_f8f6f4 v[58:61], v[8:15], v[214:221], 0
	v_mfma_f32_16x16x128_f8f6f4 v[50:53], v[0:7], v[214:221], 0
	v_mfma_f32_16x16x128_f8f6f4 v[40:43], v[8:15], v[240:247], 0
	v_mfma_f32_16x16x128_f8f6f4 v[32:35], v[0:7], v[240:247], 0
	s_setprio 0
	s_barrier
	s_add_i32 s12, 0, 0x18000
	s_add_i32 s13, 0, 0x1c000
	v_add_u32_e32 v12, s12, v192
	v_add_u32_e32 v28, s13, v192
	ds_read_b128 v[0:3], v12
	ds_read_b128 v[4:7], v12 offset:1024
	ds_read_b128 v[8:11], v12 offset:2048
	ds_read_b128 v[12:15], v12 offset:3072
	ds_read_b128 v[16:19], v28
	ds_read_b128 v[20:23], v28 offset:1024
	ds_read_b128 v[24:27], v28 offset:2048
	ds_read_b128 v[28:31], v28 offset:3072
	s_mov_b32 m0, s76
	v_lshl_add_u64 v[176:177], s[36:37], 0, v[176:177]
	ds_read_b128 v[198:201], v193 offset:32768
	ds_read_b128 v[202:205], v193 offset:33792
	ds_read_b128 v[206:209], v193 offset:34816
	ds_read_b128 v[210:213], v193 offset:35840
	ds_read_b128 v[214:217], v193 offset:36864
	ds_read_b128 v[218:221], v193 offset:37888
	ds_read_b128 v[240:243], v193 offset:38912
	ds_read_b128 v[244:247], v193 offset:39936
	global_load_lds_dwordx4 v[176:177], off
	v_lshl_add_u64 v[174:175], s[36:37], 0, v[174:175]
	s_mov_b32 m0, s77
	s_nop 0
	global_load_lds_dwordx4 v[174:175], off
	s_waitcnt vmcnt(8)
	s_waitcnt lgkmcnt(0)
	s_barrier
	s_setprio 1
	s_waitcnt lgkmcnt(0)
	v_mfma_f32_16x16x128_f8f6f4 v[158:161], v[0:7], v[198:205], v[158:161]
	v_mfma_f32_16x16x128_f8f6f4 v[150:153], v[8:15], v[198:205], v[150:153]
	v_mfma_f32_16x16x128_f8f6f4 v[142:145], v[0:7], v[206:213], v[142:145]
	v_mfma_f32_16x16x128_f8f6f4 v[134:137], v[8:15], v[206:213], v[134:137]
	v_mfma_f32_16x16x128_f8f6f4 v[126:129], v[0:7], v[214:221], v[126:129]
	v_mfma_f32_16x16x128_f8f6f4 v[118:121], v[8:15], v[214:221], v[118:121]
	v_mfma_f32_16x16x128_f8f6f4 v[110:113], v[0:7], v[240:247], v[110:113]
	v_mfma_f32_16x16x128_f8f6f4 v[102:105], v[8:15], v[240:247], v[102:105]
	s_setprio 0
	s_setprio 1
	v_mfma_f32_16x16x128_f8f6f4 v[154:157], v[16:23], v[198:205], v[154:157]
	v_mfma_f32_16x16x128_f8f6f4 v[146:149], v[24:31], v[198:205], v[146:149]
	v_mfma_f32_16x16x128_f8f6f4 v[138:141], v[16:23], v[206:213], v[138:141]
	v_mfma_f32_16x16x128_f8f6f4 v[130:133], v[24:31], v[206:213], v[130:133]
	v_mfma_f32_16x16x128_f8f6f4 v[122:125], v[16:23], v[214:221], v[122:125]
	v_mfma_f32_16x16x128_f8f6f4 v[114:117], v[24:31], v[214:221], v[114:117]
	v_mfma_f32_16x16x128_f8f6f4 v[106:109], v[16:23], v[240:247], v[106:109]
	v_mfma_f32_16x16x128_f8f6f4 v[98:101], v[24:31], v[240:247], v[98:101]
	s_setprio 0
	s_barrier
	s_add_i32 s12, s12, s49
	v_lshl_add_u64 v[174:175], v[178:179], 0, s[88:89]
	s_mov_b32 m0, s12
	ds_read_b128 v[198:201], v193 offset:49152
	ds_read_b128 v[202:205], v193 offset:50176
	ds_read_b128 v[206:209], v193 offset:51200
	ds_read_b128 v[210:213], v193 offset:52224
	ds_read_b128 v[214:217], v193 offset:53248
	ds_read_b128 v[218:221], v193 offset:54272
	ds_read_b128 v[240:243], v193 offset:55296
	ds_read_b128 v[244:247], v193 offset:56320
	global_load_lds_dwordx4 v[174:175], off
	s_add_i32 m0, s12, 0x2000
	s_add_u32 s0, s0, 0x20080
	v_lshl_add_u64 v[174:175], v[180:181], 0, s[88:89]
	s_addc_u32 s1, s1, 0
	s_add_i32 s12, s13, s49
	global_load_lds_dwordx4 v[174:175], off
	v_lshl_add_u64 v[174:175], s[0:1], 0, v[162:163]
	s_mov_b32 m0, s12
	s_nop 0
	global_load_lds_dwordx4 v[174:175], off
	v_lshl_add_u64 v[174:175], s[0:1], 0, v[164:165]
	s_add_i32 m0, s12, 0x2000
	s_nop 0
	global_load_lds_dwordx4 v[174:175], off
	v_lshl_add_u64 v[174:175], v[184:185], 0, s[88:89]
	s_mov_b32 m0, s78
	s_nop 0
	global_load_lds_dwordx4 v[174:175], off
	v_lshl_add_u64 v[174:175], v[182:183], 0, s[88:89]
	s_mov_b32 m0, s79
	s_nop 0
	global_load_lds_dwordx4 v[174:175], off
	s_waitcnt vmcnt(8)
	s_waitcnt lgkmcnt(0)
	s_barrier
	s_setprio 1
	s_waitcnt lgkmcnt(0)
	v_mfma_f32_16x16x128_f8f6f4 v[94:97], v[0:7], v[198:205], v[94:97]
	v_mfma_f32_16x16x128_f8f6f4 v[86:89], v[8:15], v[198:205], v[86:89]
	v_mfma_f32_16x16x128_f8f6f4 v[78:81], v[0:7], v[206:213], v[78:81]
	v_mfma_f32_16x16x128_f8f6f4 v[70:73], v[8:15], v[206:213], v[70:73]
	v_mfma_f32_16x16x128_f8f6f4 v[62:65], v[0:7], v[214:221], v[62:65]
	v_mfma_f32_16x16x128_f8f6f4 v[54:57], v[8:15], v[214:221], v[54:57]
	v_mfma_f32_16x16x128_f8f6f4 v[44:47], v[0:7], v[240:247], v[44:47]
	v_mfma_f32_16x16x128_f8f6f4 v[36:39], v[8:15], v[240:247], v[36:39]
	s_setprio 0
	s_setprio 1
	v_mfma_f32_16x16x128_f8f6f4 v[90:93], v[16:23], v[198:205], v[90:93]
	v_mfma_f32_16x16x128_f8f6f4 v[82:85], v[24:31], v[198:205], v[82:85]
	v_mfma_f32_16x16x128_f8f6f4 v[74:77], v[16:23], v[206:213], v[74:77]
	v_mfma_f32_16x16x128_f8f6f4 v[66:69], v[24:31], v[206:213], v[66:69]
	v_mfma_f32_16x16x128_f8f6f4 v[58:61], v[16:23], v[214:221], v[58:61]
	v_mfma_f32_16x16x128_f8f6f4 v[50:53], v[24:31], v[214:221], v[50:53]
	v_mfma_f32_16x16x128_f8f6f4 v[40:43], v[16:23], v[240:247], v[40:43]
	v_mfma_f32_16x16x128_f8f6f4 v[32:35], v[24:31], v[240:247], v[32:35]
	s_setprio 0
	s_barrier
	s_add_i32 s10, s10, 2
	s_add_u32 s70, s70, 0x100
	s_addc_u32 s71, s71, 0
	s_add_u32 s8, s8, 0x100
	s_addc_u32 s9, s9, 0
	s_cmp_gt_u32 s10, 5
	s_branch .LBB0_858

.LBB0_862:
	s_lshl_b32 s0, s68, 7
	s_mov_b32 s69, 0x48000000
	v_lshl_add_u32 v6, s6, 8, v167
	s_and_b32 s0, s0, 0x380
	v_or_b32_e32 v48, s0, v171
	s_nop 15
	s_nop 15
	s_mov_b32 s0, 0x20000
	v_mul_f32_e32 v24, 0xbab8aa3b, v158
	v_mul_f32_e32 v25, 0xbab8aa3b, v159
	v_mul_f32_e32 v26, 0xbab8aa3b, v160
	v_mul_f32_e32 v27, 0xbab8aa3b, v161
	v_mul_f32_e32 v28, 0xbab8aa3b, v150
	v_mul_f32_e32 v29, 0xbab8aa3b, v151
	v_mul_f32_e32 v30, 0xbab8aa3b, v152
	v_mul_f32_e32 v31, 0xbab8aa3b, v153
	v_exp_f32_e32 v24, v24
	v_exp_f32_e32 v25, v25
	v_exp_f32_e32 v26, v26
	v_exp_f32_e32 v27, v27
	v_exp_f32_e32 v28, v28
	v_exp_f32_e32 v29, v29
	v_exp_f32_e32 v30, v30
	v_exp_f32_e32 v31, v31
	v_mul_f32_e32 v8, v158, v154
	v_mul_f32_e32 v9, v159, v155
	v_mul_f32_e32 v10, v160, v156
	v_mul_f32_e32 v11, v161, v157
	v_mul_f32_e32 v12, v150, v146
	v_mul_f32_e32 v13, v151, v147
	v_mul_f32_e32 v14, v152, v148
	v_mul_f32_e32 v15, v153, v149
	v_fma_f32 v24, v24, s69, s69
	v_fma_f32 v25, v25, s69, s69
	v_fma_f32 v26, v26, s69, s69
	v_fma_f32 v27, v27, s69, s69
	v_fma_f32 v28, v28, s69, s69
	v_fma_f32 v29, v29, s69, s69
	v_fma_f32 v30, v30, s69, s69
	v_fma_f32 v31, v31, s69, s69
	v_rcp_f32_e32 v24, v24
	v_rcp_f32_e32 v25, v25
	v_rcp_f32_e32 v26, v26
	v_rcp_f32_e32 v27, v27
	v_rcp_f32_e32 v28, v28
	v_rcp_f32_e32 v29, v29
	v_rcp_f32_e32 v30, v30
	v_rcp_f32_e32 v31, v31
	v_mul_f32_e32 v8, v8, v24
	v_mul_f32_e32 v9, v9, v25
	v_mul_f32_e32 v10, v10, v26
	v_mul_f32_e32 v11, v11, v27
	v_mul_f32_e32 v12, v12, v28
	v_mul_f32_e32 v13, v13, v29
	v_mul_f32_e32 v14, v14, v30
	v_mul_f32_e32 v15, v15, v31
	v_med3_f32 v8, v8, s11, v232
	v_med3_f32 v9, v9, s11, v232
	v_med3_f32 v10, v10, s11, v232
	v_med3_f32 v11, v11, s11, v232
	v_med3_f32 v12, v12, s11, v232
	v_med3_f32 v13, v13, s11, v232
	v_med3_f32 v14, v14, s11, v232
	v_med3_f32 v15, v15, s11, v232
	v_mul_f32_e32 v24, 0xbab8aa3b, v142
	v_mul_f32_e32 v25, 0xbab8aa3b, v143
	v_mul_f32_e32 v26, 0xbab8aa3b, v144
	v_mul_f32_e32 v27, 0xbab8aa3b, v145
	v_mul_f32_e32 v28, 0xbab8aa3b, v134
	v_mul_f32_e32 v29, 0xbab8aa3b, v135
	v_mul_f32_e32 v30, 0xbab8aa3b, v136
	v_mul_f32_e32 v31, 0xbab8aa3b, v137
	v_exp_f32_e32 v24, v24
	v_exp_f32_e32 v25, v25
	v_exp_f32_e32 v26, v26
	v_exp_f32_e32 v27, v27
	v_exp_f32_e32 v28, v28
	v_exp_f32_e32 v29, v29
	v_exp_f32_e32 v30, v30
	v_exp_f32_e32 v31, v31
	v_mul_f32_e32 v16, v142, v138
	v_mul_f32_e32 v17, v143, v139
	v_mul_f32_e32 v18, v144, v140
	v_mul_f32_e32 v19, v145, v141
	v_mul_f32_e32 v20, v134, v130
	v_mul_f32_e32 v21, v135, v131
	v_mul_f32_e32 v22, v136, v132
	v_mul_f32_e32 v23, v137, v133
	v_fma_f32 v24, v24, s69, s69
	v_fma_f32 v25, v25, s69, s69
	v_fma_f32 v26, v26, s69, s69
	v_fma_f32 v27, v27, s69, s69
	v_fma_f32 v28, v28, s69, s69
	v_fma_f32 v29, v29, s69, s69
	v_fma_f32 v30, v30, s69, s69
	v_fma_f32 v31, v31, s69, s69
	v_rcp_f32_e32 v24, v24
	v_rcp_f32_e32 v25, v25
	v_rcp_f32_e32 v26, v26
	v_rcp_f32_e32 v27, v27
	v_rcp_f32_e32 v28, v28
	v_rcp_f32_e32 v29, v29
	v_rcp_f32_e32 v30, v30
	v_rcp_f32_e32 v31, v31
	v_mul_f32_e32 v16, v16, v24
	v_mul_f32_e32 v17, v17, v25
	v_mul_f32_e32 v18, v18, v26
	v_mul_f32_e32 v19, v19, v27
	v_mul_f32_e32 v20, v20, v28
	v_mul_f32_e32 v21, v21, v29
	v_mul_f32_e32 v22, v22, v30
	v_mul_f32_e32 v23, v23, v31
	v_med3_f32 v16, v16, s11, v232
	v_med3_f32 v17, v17, s11, v232
	v_med3_f32 v18, v18, s11, v232
	v_med3_f32 v19, v19, s11, v232
	v_med3_f32 v20, v20, s11, v232
	v_med3_f32 v21, v21, s11, v232
	v_med3_f32 v22, v22, s11, v232
	v_med3_f32 v23, v23, s11, v232
	v_cvt_pk_fp8_f32 v0, v8, v9
	v_cvt_pk_fp8_f32 v1, v12, v13
	v_cvt_pk_fp8_f32 v2, v16, v17
	v_cvt_pk_fp8_f32 v3, v20, v21
	v_cvt_pk_fp8_f32 v0, v10, v11 op_sel:[0,0,1]
	v_cvt_pk_fp8_f32 v1, v14, v15 op_sel:[0,0,1]
	v_cvt_pk_fp8_f32 v2, v18, v19 op_sel:[0,0,1]
	v_cvt_pk_fp8_f32 v3, v22, v23 op_sel:[0,0,1]
	v_ashrrev_i32_e32 v7, 31, v6
	v_lshlrev_b64 v[4:5], 10, v[6:7]
	v_lshl_add_u64 v[4:5], s[58:59], 0, v[4:5]
	v_lshl_add_u64 v[4:5], v[4:5], 0, v[48:49]
	s_nop 1
	v_permlane16_swap_b32_e32 v0, v2
	v_permlane16_swap_b32_e32 v1, v3
	global_store_dwordx4 v[4:5], v[0:3], off
	v_or_b32_e32 v6, 32, v6
	v_mul_f32_e32 v24, 0xbab8aa3b, v126
	v_mul_f32_e32 v25, 0xbab8aa3b, v127
	v_mul_f32_e32 v26, 0xbab8aa3b, v128
	v_mul_f32_e32 v27, 0xbab8aa3b, v129
	v_mul_f32_e32 v28, 0xbab8aa3b, v118
	v_mul_f32_e32 v29, 0xbab8aa3b, v119
	v_mul_f32_e32 v30, 0xbab8aa3b, v120
	v_mul_f32_e32 v31, 0xbab8aa3b, v121
	v_exp_f32_e32 v24, v24
	v_exp_f32_e32 v25, v25
	v_exp_f32_e32 v26, v26
	v_exp_f32_e32 v27, v27
	v_exp_f32_e32 v28, v28
	v_exp_f32_e32 v29, v29
	v_exp_f32_e32 v30, v30
	v_exp_f32_e32 v31, v31
	v_mul_f32_e32 v8, v126, v122
	v_mul_f32_e32 v9, v127, v123
	v_mul_f32_e32 v10, v128, v124
	v_mul_f32_e32 v11, v129, v125
	v_mul_f32_e32 v12, v118, v114
	v_mul_f32_e32 v13, v119, v115
	v_mul_f32_e32 v14, v120, v116
	v_mul_f32_e32 v15, v121, v117
	v_fma_f32 v24, v24, s69, s69
	v_fma_f32 v25, v25, s69, s69
	v_fma_f32 v26, v26, s69, s69
	v_fma_f32 v27, v27, s69, s69
	v_fma_f32 v28, v28, s69, s69
	v_fma_f32 v29, v29, s69, s69
	v_fma_f32 v30, v30, s69, s69
	v_fma_f32 v31, v31, s69, s69
	v_rcp_f32_e32 v24, v24
	v_rcp_f32_e32 v25, v25
	v_rcp_f32_e32 v26, v26
	v_rcp_f32_e32 v27, v27
	v_rcp_f32_e32 v28, v28
	v_rcp_f32_e32 v29, v29
	v_rcp_f32_e32 v30, v30
	v_rcp_f32_e32 v31, v31
	v_mul_f32_e32 v8, v8, v24
	v_mul_f32_e32 v9, v9, v25
	v_mul_f32_e32 v10, v10, v26
	v_mul_f32_e32 v11, v11, v27
	v_mul_f32_e32 v12, v12, v28
	v_mul_f32_e32 v13, v13, v29
	v_mul_f32_e32 v14, v14, v30
	v_mul_f32_e32 v15, v15, v31
	v_med3_f32 v8, v8, s11, v232
	v_med3_f32 v9, v9, s11, v232
	v_med3_f32 v10, v10, s11, v232
	v_med3_f32 v11, v11, s11, v232
	v_med3_f32 v12, v12, s11, v232
	v_med3_f32 v13, v13, s11, v232
	v_med3_f32 v14, v14, s11, v232
	v_med3_f32 v15, v15, s11, v232
	v_mul_f32_e32 v24, 0xbab8aa3b, v110
	v_mul_f32_e32 v25, 0xbab8aa3b, v111
	v_mul_f32_e32 v26, 0xbab8aa3b, v112
	v_mul_f32_e32 v27, 0xbab8aa3b, v113
	v_mul_f32_e32 v28, 0xbab8aa3b, v102
	v_mul_f32_e32 v29, 0xbab8aa3b, v103
	v_mul_f32_e32 v30, 0xbab8aa3b, v104
	v_mul_f32_e32 v31, 0xbab8aa3b, v105
	v_exp_f32_e32 v24, v24
	v_exp_f32_e32 v25, v25
	v_exp_f32_e32 v26, v26
	v_exp_f32_e32 v27, v27
	v_exp_f32_e32 v28, v28
	v_exp_f32_e32 v29, v29
	v_exp_f32_e32 v30, v30
	v_exp_f32_e32 v31, v31
	v_mul_f32_e32 v16, v110, v106
	v_mul_f32_e32 v17, v111, v107
	v_mul_f32_e32 v18, v112, v108
	v_mul_f32_e32 v19, v113, v109
	v_mul_f32_e32 v20, v102, v98
	v_mul_f32_e32 v21, v103, v99
	v_mul_f32_e32 v22, v104, v100
	v_mul_f32_e32 v23, v105, v101
	v_fma_f32 v24, v24, s69, s69
	v_fma_f32 v25, v25, s69, s69
	v_fma_f32 v26, v26, s69, s69
	v_fma_f32 v27, v27, s69, s69
	v_fma_f32 v28, v28, s69, s69
	v_fma_f32 v29, v29, s69, s69
	v_fma_f32 v30, v30, s69, s69
	v_fma_f32 v31, v31, s69, s69
	v_rcp_f32_e32 v24, v24
	v_rcp_f32_e32 v25, v25
	v_rcp_f32_e32 v26, v26
	v_rcp_f32_e32 v27, v27
	v_rcp_f32_e32 v28, v28
	v_rcp_f32_e32 v29, v29
	v_rcp_f32_e32 v30, v30
	v_rcp_f32_e32 v31, v31
	v_mul_f32_e32 v16, v16, v24
	v_mul_f32_e32 v17, v17, v25
	v_mul_f32_e32 v18, v18, v26
	v_mul_f32_e32 v19, v19, v27
	v_mul_f32_e32 v20, v20, v28
	v_mul_f32_e32 v21, v21, v29
	v_mul_f32_e32 v22, v22, v30
	v_mul_f32_e32 v23, v23, v31
	v_med3_f32 v16, v16, s11, v232
	v_med3_f32 v17, v17, s11, v232
	v_med3_f32 v18, v18, s11, v232
	v_med3_f32 v19, v19, s11, v232
	v_med3_f32 v20, v20, s11, v232
	v_med3_f32 v21, v21, s11, v232
	v_med3_f32 v22, v22, s11, v232
	v_med3_f32 v23, v23, s11, v232
	v_cvt_pk_fp8_f32 v0, v8, v9
	v_cvt_pk_fp8_f32 v1, v12, v13
	v_cvt_pk_fp8_f32 v2, v16, v17
	v_cvt_pk_fp8_f32 v3, v20, v21
	v_cvt_pk_fp8_f32 v0, v10, v11 op_sel:[0,0,1]
	v_cvt_pk_fp8_f32 v1, v14, v15 op_sel:[0,0,1]
	v_cvt_pk_fp8_f32 v2, v18, v19 op_sel:[0,0,1]
	v_cvt_pk_fp8_f32 v3, v22, v23 op_sel:[0,0,1]
	v_ashrrev_i32_e32 v7, 31, v6
	v_lshlrev_b64 v[6:7], 10, v[6:7]
	v_lshl_add_u64 v[6:7], s[58:59], 0, v[6:7]
	v_lshl_add_u64 v[6:7], v[6:7], 0, v[48:49]
	s_nop 1
	v_permlane16_swap_b32_e32 v0, v2
	v_permlane16_swap_b32_e32 v1, v3
	global_store_dwordx4 v[6:7], v[0:3], off
	v_mul_f32_e32 v24, 0xbab8aa3b, v94
	v_mul_f32_e32 v25, 0xbab8aa3b, v95
	v_mul_f32_e32 v26, 0xbab8aa3b, v96
	v_mul_f32_e32 v27, 0xbab8aa3b, v97
	v_mul_f32_e32 v28, 0xbab8aa3b, v86
	v_mul_f32_e32 v29, 0xbab8aa3b, v87
	v_mul_f32_e32 v30, 0xbab8aa3b, v88
	v_mul_f32_e32 v31, 0xbab8aa3b, v89
	v_exp_f32_e32 v24, v24
	v_exp_f32_e32 v25, v25
	v_exp_f32_e32 v26, v26
	v_exp_f32_e32 v27, v27
	v_exp_f32_e32 v28, v28
	v_exp_f32_e32 v29, v29
	v_exp_f32_e32 v30, v30
	v_exp_f32_e32 v31, v31
	v_mul_f32_e32 v8, v94, v90
	v_mul_f32_e32 v9, v95, v91
	v_mul_f32_e32 v10, v96, v92
	v_mul_f32_e32 v11, v97, v93
	v_mul_f32_e32 v12, v86, v82
	v_mul_f32_e32 v13, v87, v83
	v_mul_f32_e32 v14, v88, v84
	v_mul_f32_e32 v15, v89, v85
	v_fma_f32 v24, v24, s69, s69
	v_fma_f32 v25, v25, s69, s69
	v_fma_f32 v26, v26, s69, s69
	v_fma_f32 v27, v27, s69, s69
	v_fma_f32 v28, v28, s69, s69
	v_fma_f32 v29, v29, s69, s69
	v_fma_f32 v30, v30, s69, s69
	v_fma_f32 v31, v31, s69, s69
	v_rcp_f32_e32 v24, v24
	v_rcp_f32_e32 v25, v25
	v_rcp_f32_e32 v26, v26
	v_rcp_f32_e32 v27, v27
	v_rcp_f32_e32 v28, v28
	v_rcp_f32_e32 v29, v29
	v_rcp_f32_e32 v30, v30
	v_rcp_f32_e32 v31, v31
	v_mul_f32_e32 v8, v8, v24
	v_mul_f32_e32 v9, v9, v25
	v_mul_f32_e32 v10, v10, v26
	v_mul_f32_e32 v11, v11, v27
	v_mul_f32_e32 v12, v12, v28
	v_mul_f32_e32 v13, v13, v29
	v_mul_f32_e32 v14, v14, v30
	v_mul_f32_e32 v15, v15, v31
	v_med3_f32 v8, v8, s11, v232
	v_med3_f32 v9, v9, s11, v232
	v_med3_f32 v10, v10, s11, v232
	v_med3_f32 v11, v11, s11, v232
	v_med3_f32 v12, v12, s11, v232
	v_med3_f32 v13, v13, s11, v232
	v_med3_f32 v14, v14, s11, v232
	v_med3_f32 v15, v15, s11, v232
	v_mul_f32_e32 v24, 0xbab8aa3b, v78
	v_mul_f32_e32 v25, 0xbab8aa3b, v79
	v_mul_f32_e32 v26, 0xbab8aa3b, v80
	v_mul_f32_e32 v27, 0xbab8aa3b, v81
	v_mul_f32_e32 v28, 0xbab8aa3b, v70
	v_mul_f32_e32 v29, 0xbab8aa3b, v71
	v_mul_f32_e32 v30, 0xbab8aa3b, v72
	v_mul_f32_e32 v31, 0xbab8aa3b, v73
	v_exp_f32_e32 v24, v24
	v_exp_f32_e32 v25, v25
	v_exp_f32_e32 v26, v26
	v_exp_f32_e32 v27, v27
	v_exp_f32_e32 v28, v28
	v_exp_f32_e32 v29, v29
	v_exp_f32_e32 v30, v30
	v_exp_f32_e32 v31, v31
	v_mul_f32_e32 v16, v78, v74
	v_mul_f32_e32 v17, v79, v75
	v_mul_f32_e32 v18, v80, v76
	v_mul_f32_e32 v19, v81, v77
	v_mul_f32_e32 v20, v70, v66
	v_mul_f32_e32 v21, v71, v67
	v_mul_f32_e32 v22, v72, v68
	v_mul_f32_e32 v23, v73, v69
	v_fma_f32 v24, v24, s69, s69
	v_fma_f32 v25, v25, s69, s69
	v_fma_f32 v26, v26, s69, s69
	v_fma_f32 v27, v27, s69, s69
	v_fma_f32 v28, v28, s69, s69
	v_fma_f32 v29, v29, s69, s69
	v_fma_f32 v30, v30, s69, s69
	v_fma_f32 v31, v31, s69, s69
	v_rcp_f32_e32 v24, v24
	v_rcp_f32_e32 v25, v25
	v_rcp_f32_e32 v26, v26
	v_rcp_f32_e32 v27, v27
	v_rcp_f32_e32 v28, v28
	v_rcp_f32_e32 v29, v29
	v_rcp_f32_e32 v30, v30
	v_rcp_f32_e32 v31, v31
	v_mul_f32_e32 v16, v16, v24
	v_mul_f32_e32 v17, v17, v25
	v_mul_f32_e32 v18, v18, v26
	v_mul_f32_e32 v19, v19, v27
	v_mul_f32_e32 v20, v20, v28
	v_mul_f32_e32 v21, v21, v29
	v_mul_f32_e32 v22, v22, v30
	v_mul_f32_e32 v23, v23, v31
	v_med3_f32 v16, v16, s11, v232
	v_med3_f32 v17, v17, s11, v232
	v_med3_f32 v18, v18, s11, v232
	v_med3_f32 v19, v19, s11, v232
	v_med3_f32 v20, v20, s11, v232
	v_med3_f32 v21, v21, s11, v232
	v_med3_f32 v22, v22, s11, v232
	v_med3_f32 v23, v23, s11, v232
	v_cvt_pk_fp8_f32 v0, v8, v9
	v_cvt_pk_fp8_f32 v1, v12, v13
	v_cvt_pk_fp8_f32 v2, v16, v17
	v_cvt_pk_fp8_f32 v3, v20, v21
	v_cvt_pk_fp8_f32 v0, v10, v11 op_sel:[0,0,1]
	v_cvt_pk_fp8_f32 v1, v14, v15 op_sel:[0,0,1]
	v_cvt_pk_fp8_f32 v2, v18, v19 op_sel:[0,0,1]
	v_cvt_pk_fp8_f32 v3, v22, v23 op_sel:[0,0,1]
	v_add_co_u32_e32 v6, vcc, s0, v4
	s_nop 1
	v_addc_co_u32_e32 v7, vcc, 0, v5, vcc
	s_nop 1
	v_permlane16_swap_b32_e32 v0, v2
	v_permlane16_swap_b32_e32 v1, v3
	global_store_dwordx4 v[6:7], v[0:3], off
	v_mul_f32_e32 v24, 0xbab8aa3b, v62
	v_mul_f32_e32 v25, 0xbab8aa3b, v63
	v_mul_f32_e32 v26, 0xbab8aa3b, v64
	v_mul_f32_e32 v27, 0xbab8aa3b, v65
	v_mul_f32_e32 v28, 0xbab8aa3b, v54
	v_mul_f32_e32 v29, 0xbab8aa3b, v55
	v_mul_f32_e32 v30, 0xbab8aa3b, v56
	v_mul_f32_e32 v31, 0xbab8aa3b, v57
	v_exp_f32_e32 v24, v24
	v_exp_f32_e32 v25, v25
	v_exp_f32_e32 v26, v26
	v_exp_f32_e32 v27, v27
	v_exp_f32_e32 v28, v28
	v_exp_f32_e32 v29, v29
	v_exp_f32_e32 v30, v30
	v_exp_f32_e32 v31, v31
	v_mul_f32_e32 v8, v62, v58
	v_mul_f32_e32 v9, v63, v59
	v_mul_f32_e32 v10, v64, v60
	v_mul_f32_e32 v11, v65, v61
	v_mul_f32_e32 v12, v54, v50
	v_mul_f32_e32 v13, v55, v51
	v_mul_f32_e32 v14, v56, v52
	v_mul_f32_e32 v15, v57, v53
	v_fma_f32 v24, v24, s69, s69
	v_fma_f32 v25, v25, s69, s69
	v_fma_f32 v26, v26, s69, s69
	v_fma_f32 v27, v27, s69, s69
	v_fma_f32 v28, v28, s69, s69
	v_fma_f32 v29, v29, s69, s69
	v_fma_f32 v30, v30, s69, s69
	v_fma_f32 v31, v31, s69, s69
	v_rcp_f32_e32 v24, v24
	v_rcp_f32_e32 v25, v25
	v_rcp_f32_e32 v26, v26
	v_rcp_f32_e32 v27, v27
	v_rcp_f32_e32 v28, v28
	v_rcp_f32_e32 v29, v29
	v_rcp_f32_e32 v30, v30
	v_rcp_f32_e32 v31, v31
	v_mul_f32_e32 v8, v8, v24
	v_mul_f32_e32 v9, v9, v25
	v_mul_f32_e32 v10, v10, v26
	v_mul_f32_e32 v11, v11, v27
	v_mul_f32_e32 v12, v12, v28
	v_mul_f32_e32 v13, v13, v29
	v_mul_f32_e32 v14, v14, v30
	v_mul_f32_e32 v15, v15, v31
	v_med3_f32 v8, v8, s11, v232
	v_med3_f32 v9, v9, s11, v232
	v_med3_f32 v10, v10, s11, v232
	v_med3_f32 v11, v11, s11, v232
	v_med3_f32 v12, v12, s11, v232
	v_med3_f32 v13, v13, s11, v232
	v_med3_f32 v14, v14, s11, v232
	v_med3_f32 v15, v15, s11, v232
	v_mul_f32_e32 v24, 0xbab8aa3b, v44
	v_mul_f32_e32 v25, 0xbab8aa3b, v45
	v_mul_f32_e32 v26, 0xbab8aa3b, v46
	v_mul_f32_e32 v27, 0xbab8aa3b, v47
	v_mul_f32_e32 v28, 0xbab8aa3b, v36
	v_mul_f32_e32 v29, 0xbab8aa3b, v37
	v_mul_f32_e32 v30, 0xbab8aa3b, v38
	v_mul_f32_e32 v31, 0xbab8aa3b, v39
	v_exp_f32_e32 v24, v24
	v_exp_f32_e32 v25, v25
	v_exp_f32_e32 v26, v26
	v_exp_f32_e32 v27, v27
	v_exp_f32_e32 v28, v28
	v_exp_f32_e32 v29, v29
	v_exp_f32_e32 v30, v30
	v_exp_f32_e32 v31, v31
	v_mul_f32_e32 v16, v44, v40
	v_mul_f32_e32 v17, v45, v41
	v_mul_f32_e32 v18, v46, v42
	v_mul_f32_e32 v19, v47, v43
	v_mul_f32_e32 v20, v36, v32
	v_mul_f32_e32 v21, v37, v33
	v_mul_f32_e32 v22, v38, v34
	v_mul_f32_e32 v23, v39, v35
	v_fma_f32 v24, v24, s69, s69
	v_fma_f32 v25, v25, s69, s69
	v_fma_f32 v26, v26, s69, s69
	v_fma_f32 v27, v27, s69, s69
	v_fma_f32 v28, v28, s69, s69
	v_fma_f32 v29, v29, s69, s69
	v_fma_f32 v30, v30, s69, s69
	v_fma_f32 v31, v31, s69, s69
	v_rcp_f32_e32 v24, v24
	v_rcp_f32_e32 v25, v25
	v_rcp_f32_e32 v26, v26
	v_rcp_f32_e32 v27, v27
	v_rcp_f32_e32 v28, v28
	v_rcp_f32_e32 v29, v29
	v_rcp_f32_e32 v30, v30
	v_rcp_f32_e32 v31, v31
	v_mul_f32_e32 v16, v16, v24
	v_mul_f32_e32 v17, v17, v25
	v_mul_f32_e32 v18, v18, v26
	v_mul_f32_e32 v19, v19, v27
	v_mul_f32_e32 v20, v20, v28
	v_mul_f32_e32 v21, v21, v29
	v_mul_f32_e32 v22, v22, v30
	v_mul_f32_e32 v23, v23, v31
	v_med3_f32 v16, v16, s11, v232
	v_med3_f32 v17, v17, s11, v232
	v_med3_f32 v18, v18, s11, v232
	v_med3_f32 v19, v19, s11, v232
	v_med3_f32 v20, v20, s11, v232
	v_med3_f32 v21, v21, s11, v232
	v_med3_f32 v22, v22, s11, v232
	v_med3_f32 v23, v23, s11, v232
	v_cvt_pk_fp8_f32 v0, v8, v9
	v_cvt_pk_fp8_f32 v1, v12, v13
	v_cvt_pk_fp8_f32 v2, v16, v17
	v_cvt_pk_fp8_f32 v3, v20, v21
	v_cvt_pk_fp8_f32 v0, v10, v11 op_sel:[0,0,1]
	v_cvt_pk_fp8_f32 v1, v14, v15 op_sel:[0,0,1]
	v_cvt_pk_fp8_f32 v2, v18, v19 op_sel:[0,0,1]
	v_cvt_pk_fp8_f32 v3, v22, v23 op_sel:[0,0,1]
	v_add_co_u32_e32 v4, vcc, 0x28000, v4
	s_nop 1
	v_addc_co_u32_e32 v5, vcc, 0, v5, vcc
	s_mov_b64 s[0:1], -1
	s_nop 1
	v_permlane16_swap_b32_e32 v0, v2
	v_permlane16_swap_b32_e32 v1, v3
	s_andn2_b64 vcc, exec, s[38:39]
	global_store_dwordx4 v[4:5], v[0:3], off
	s_cbranch_vccnz .LBB0_849
	s_andn2_b64 vcc, exec, s[56:57]
	s_cbranch_vccnz .LBB0_848
	s_barrier
	s_branch .LBB0_848
